# GLA: the e4m3 output scale (x4, a power of two) is carried by the query scale (1/8 -> 1/2) instead of 16 multiplies per chunk on the output tile (bit-identical values)
# speedup vs baseline: 1.0043x; 1.0007x over previous
.Lgp_skip:
	v_add_f32_e32 v32, 0, v117
	v_add_u32_e32 v210, s98, v210
	global_load_short_d16_hi v178, v210, s[80:81]
	v_add_f32_e32 v40, v32, v120
	v_add_f32_e32 v41, v40, v123
	global_load_short_d16_hi v179, v210, s[80:81] offset:512
	v_add_f32_e32 v42, v41, v128
	v_add_f32_e32 v43, v42, v131
	v_add_f32_e32 v44, v43, v134
	v_add_u32_e32 v211, s99, v211
	global_load_short_d16_hi v180, v211, s[78:79]
	v_add_f32_e32 v45, v44, v137
	v_add_f32_e32 v33, v45, v140
	v_add_u32_e32 v30, s86, v91
	v_add_u32_e32 v210, s98, v210
	global_load_short_d16_hi v181, v210, s[80:81]
	ds_write_b32 v30, v33 offset:46080
	s_waitcnt lgkmcnt(0)
	s_barrier
	ds_read2st64_b32 v[30:31], v91 offset0:180 offset1:181
	ds_read2st64_b32 v[248:249], v91 offset0:182 offset1:183
	ds_read2st64_b32 v[250:251], v91 offset0:184 offset1:185
	ds_read2st64_b32 v[252:253], v91 offset0:186 offset1:187
	global_load_short_d16_hi v182, v210, s[80:81] offset:512
	v_mul_f32_e32 v47, 0.5, v115
	s_andn2_b64 vcc, exec, s[18:19]
	s_waitcnt lgkmcnt(0)
	v_add_f32_e32 v30, 0, v30
	v_cndmask_b32_e64 v35, 0, v30, s[42:43]
	v_add_u32_e32 v211, s99, v211
	global_load_short_d16_hi v183, v211, s[78:79]
	v_add_f32_e32 v46, v30, v31
	v_add_f32_e32 v30, v31, v35
	v_cndmask_b32_e64 v35, v35, v30, s[44:45]
	v_add_u32_e32 v210, s98, v210
	global_load_short_d16_hi v184, v210, s[80:81]
	v_add_f32_e32 v46, v46, v248
	v_add_f32_e32 v30, v248, v35
	v_cndmask_b32_e64 v30, v35, v30, s[46:47]
	v_add_f32_e32 v35, v46, v249
	v_add_f32_e32 v31, v249, v30
	global_load_short_d16_hi v185, v210, s[80:81] offset:512
	v_cndmask_b32_e64 v46, v30, v31, s[48:49]
	v_add_f32_e32 v35, v35, v250
	v_add_f32_e32 v30, v250, v46
	v_add_u32_e32 v211, s99, v211
	global_load_short_d16_hi v186, v211, s[78:79]
	v_cndmask_b32_e64 v30, v46, v30, s[50:51]
	v_add_f32_e32 v35, v35, v251
	v_add_f32_e32 v31, v251, v30
	v_cndmask_b32_e64 v46, v30, v31, s[52:53]
	v_add_u32_e32 v210, s98, v210
	global_load_short_d16_hi v187, v210, s[80:81]
	v_add_f32_e32 v35, v35, v252
	v_add_f32_e32 v30, v252, v46
	v_cndmask_b32_e64 v30, v46, v30, s[54:55]
	v_add_f32_e32 v35, v35, v253
	v_add_f32_e32 v31, v253, v30
	global_load_short_d16_hi v188, v210, s[80:81] offset:512
	v_cndmask_b32_e64 v46, v30, v31, s[56:57]
	v_mul_f32_e32 v30, 0x3fb8aa3b, v35
	v_exp_f32_e32 v35, v30
	v_add_f32_e32 v30, v32, v46
	v_mul_f32_e32 v30, 0x3fb8aa3b, v30
	v_add_u32_e32 v211, s99, v211
	global_load_short_d16_hi v189, v211, s[78:79]
	v_exp_f32_e32 v30, v30
	v_add_f32_e32 v33, v33, v46
	v_mul_f32_e32 v33, 0x3fb8aa3b, v33
	v_exp_f32_e32 v33, v33
	v_rcp_f32_e32 v31, v30
	v_add_u32_e32 v210, s98, v210
	global_load_short_d16_hi v190, v210, s[80:81]
	v_mul_f32_e32 v30, v47, v30
	v_cvt_pk_bf16_f32 v30, v30, s0
	s_mul_i32 s0, s71, 0x480
	v_add_u32_e32 v47, s0, v92
	v_mul_f32_e32 v32, v35, v31
	global_load_short_d16_hi v192, v210, s[80:81] offset:512
	ds_write_b16 v47, v30
	v_mul_f32_e32 v30, v31, v116
	v_add_f32_e32 v31, v40, v46
	v_mul_f32_e32 v31, 0x3fb8aa3b, v31
	v_exp_f32_e32 v31, v31
	v_add_u32_e32 v211, s99, v211
	global_load_short_d16_hi v194, v211, s[78:79]
	v_cvt_pk_bf16_f32 v30, v30, s0
	ds_write_b16 v47, v30 offset:9216
	v_mul_f32_e32 v30, v32, v116
	v_rcp_f32_e32 v32, v31
	v_add_u32_e32 v210, s98, v210
	global_load_short_d16_hi v196, v210, s[80:81]
	v_mul_f32_e32 v40, 0.5, v118
	v_mul_f32_e32 v31, v40, v31
	v_cvt_pk_bf16_f32 v31, v31, s0
	ds_write_b16 v47, v31 offset:144
	global_load_short_d16_hi v200, v210, s[80:81] offset:512
	v_mul_f32_e32 v31, v32, v119
	v_cvt_pk_bf16_f32 v31, v31, s0
	ds_write_b16 v47, v31 offset:9360
	v_mul_f32_e32 v31, v35, v32
	v_mul_f32_e32 v31, v31, v119
	v_add_u32_e32 v211, s99, v211
	global_load_short_d16_hi v201, v211, s[78:79]
	v_cvt_pk_bf16_f32 v31, v31, 0
	v_cvt_pk_bf16_f32 v30, v30, 0
	v_lshlrev_b32_e32 v31, 16, v31
	v_and_or_b32 v30, v30, s27, v31
	v_add_f32_e32 v31, v41, v46
	v_add_u32_e32 v210, s98, v210
	global_load_short_d16_hi v202, v210, s[80:81]
	v_mul_f32_e32 v31, 0x3fb8aa3b, v31
	v_exp_f32_e32 v31, v31
	v_mul_f32_e32 v41, 0.5, v121
	global_load_short_d16_hi v203, v210, s[80:81] offset:512
	v_rcp_f32_e32 v32, v31
	v_mul_f32_e32 v31, v41, v31
	v_cvt_pk_bf16_f32 v31, v31, s0
	ds_write_b16 v47, v31 offset:288
	v_mul_f32_e32 v40, v35, v32
	v_add_u32_e32 v211, s99, v211
	global_load_short_d16_hi v206, v211, s[78:79]
	v_mul_f32_e32 v31, v32, v122
	v_add_f32_e32 v32, v42, v46
	v_mul_f32_e32 v32, 0x3fb8aa3b, v32
	v_exp_f32_e32 v32, v32
	v_cvt_pk_bf16_f32 v31, v31, s0
	v_add_u32_e32 v210, s98, v210
	global_load_short_d16_hi v207, v210, s[80:81]
	ds_write_b16 v47, v31 offset:9504
	v_mul_f32_e32 v31, v40, v122
	v_rcp_f32_e32 v40, v32
	v_mul_f32_e32 v41, 0.5, v124
	global_load_short_d16_hi v208, v210, s[80:81] offset:512
	v_mul_f32_e32 v32, v41, v32
	v_cvt_pk_bf16_f32 v32, v32, s0
	ds_write_b16 v47, v32 offset:432
	v_mul_f32_e32 v32, v40, v125
	v_add_u32_e32 v211, s99, v211
	global_load_short_d16_hi v209, v211, s[78:79]
	v_cvt_pk_bf16_f32 v32, v32, s0
	ds_write_b16 v47, v32 offset:9648
	v_mul_f32_e32 v32, v35, v40
	v_mul_f32_e32 v32, v32, v125
	v_cvt_pk_bf16_f32 v32, v32, 0
	v_add_u32_e32 v214, s100, v214
	global_load_ushort v220, v214, s[80:81]
	v_cvt_pk_bf16_f32 v31, v31, 0
	v_lshlrev_b32_e32 v32, 16, v32
	v_and_or_b32 v31, v31, s27, v32
	v_add_f32_e32 v32, v43, v46
	v_mul_f32_e32 v32, 0x3fb8aa3b, v32
	v_add_u32_e32 v214, s100, v214
	global_load_ushort v219, v214, s[80:81]
	v_exp_f32_e32 v32, v32
	v_mul_f32_e32 v42, 0.5, v129
	v_rcp_f32_e32 v40, v32
	v_add_u32_e32 v214, s100, v214
	global_load_ushort v222, v214, s[80:81]
	v_mul_f32_e32 v32, v42, v32
	v_cvt_pk_bf16_f32 v32, v32, s0
	ds_write_b16 v47, v32 offset:576
	v_mul_f32_e32 v41, v35, v40
	v_mul_f32_e32 v32, v40, v130
	v_add_u32_e32 v214, s100, v214
	global_load_ushort v221, v214, s[80:81]
	v_add_f32_e32 v40, v44, v46
	v_mul_f32_e32 v40, 0x3fb8aa3b, v40
	v_exp_f32_e32 v40, v40
	v_cvt_pk_bf16_f32 v32, v32, s0
	ds_write_b16 v47, v32 offset:9792
	v_add_u32_e32 v214, s100, v214
	global_load_ushort v224, v214, s[80:81]
	v_mul_f32_e32 v32, v41, v130
	v_rcp_f32_e32 v41, v40
	v_mul_f32_e32 v42, 0.5, v132
	v_mul_f32_e32 v40, v42, v40
	v_add_u32_e32 v214, s100, v214
	global_load_ushort v223, v214, s[80:81]
	v_cvt_pk_bf16_f32 v40, v40, s0
	ds_write_b16 v47, v40 offset:720
	v_mul_f32_e32 v40, v41, v133
	v_cvt_pk_bf16_f32 v40, v40, s0
	ds_write_b16 v47, v40 offset:9936
	v_add_u32_e32 v214, s100, v214
	global_load_ushort v226, v214, s[80:81]
	v_mul_f32_e32 v40, v35, v41
	v_mul_f32_e32 v40, v40, v133
	v_cvt_pk_bf16_f32 v40, v40, 0
	v_cvt_pk_bf16_f32 v32, v32, 0
	v_lshlrev_b32_e32 v40, 16, v40
	v_add_u32_e32 v214, s100, v214
	global_load_ushort v225, v214, s[80:81]
	v_and_or_b32 v32, v32, s27, v40
	v_add_f32_e32 v40, v45, v46
	v_mul_f32_e32 v40, 0x3fb8aa3b, v40
	v_exp_f32_e32 v40, v40
	v_add_u32_e32 v214, s100, v214
	global_load_ushort v228, v214, s[80:81]
	v_mul_f32_e32 v43, 0.5, v135
	v_rcp_f32_e32 v41, v40
	v_mul_f32_e32 v40, v43, v40
	v_cvt_pk_bf16_f32 v40, v40, s0
	v_add_u32_e32 v214, s100, v214
	global_load_ushort v227, v214, s[80:81]
	ds_write_b16 v47, v40 offset:864
	v_mul_f32_e32 v40, v41, v136
	v_mul_f32_e32 v42, v35, v41
	v_cvt_pk_bf16_f32 v40, v40, s0
	ds_write_b16 v47, v40 offset:10080
	v_add_u32_e32 v214, s100, v214
	global_load_ushort v230, v214, s[80:81]
	v_mul_f32_e32 v40, v42, v136
	v_rcp_f32_e32 v41, v33
	v_mul_f32_e32 v42, 0.5, v138
	v_mul_f32_e32 v33, v42, v33
	v_add_u32_e32 v214, s100, v214
	global_load_ushort v229, v214, s[80:81]
	v_cvt_pk_bf16_f32 v33, v33, s0
	ds_write_b16 v47, v33 offset:1008
	v_mul_f32_e32 v33, v41, v139
	v_cvt_pk_bf16_f32 v33, v33, s0
	v_add_u32_e32 v214, s100, v214
	global_load_ushort v232, v214, s[80:81]
	ds_write_b16 v47, v33 offset:10224
	v_mul_f32_e32 v33, v35, v41
	v_mul_f32_e32 v33, v33, v139
	v_cvt_pk_bf16_f32 v33, v33, 0
	v_cvt_pk_bf16_f32 v40, v40, 0
	v_add_u32_e32 v214, s100, v214
	global_load_ushort v231, v214, s[80:81]
	v_lshlrev_b32_e32 v33, 16, v33
	v_and_or_b32 v33, v40, s27, v33
	v_add_u32_e32 v40, s87, v93
	ds_write_b128 v40, v[30:33] offset:18432
	s_cbranch_vccnz .LBB0_471
	ds_write_b32 v109, v35 offset:48128

.Lgo_pos:
	v_lshl_add_u32 v251, v215, 9, v218
	v_add_u32_e32 v252, s0, v251
	v_add_u32_e32 v253, s1, v251
	v_add_u32_e32 v216, s1, v252
	ds_read_b128 v[30:33], v97 offset:9216
	ds_read_b128 v[40:43], v97 offset:9280
	ds_read_b128 v[44:47], v97 offset:11520
	ds_read_b128 v[52:55], v97 offset:2304
	ds_read_b128 v[60:63], v97 offset:11584
	ds_read_b128 v[64:67], v97 offset:2368
	ds_read_b128 v[72:75], v98 offset:9216
	ds_read_b128 v[142:145], v98
	ds_read_b128 v[146:149], v98 offset:9280
	ds_read_b128 v[150:153], v98 offset:64
	ds_read_b128 v[154:157], v99 offset:9216
	ds_read_b128 v[158:161], v99
	ds_read_b128 v[162:165], v99 offset:9280
	ds_read_b128 v[166:169], v99 offset:64
	ds_read_b128 v[48:51], v97 offset:64
	ds_read_b128 v[56:59], v97
	s_waitcnt lgkmcnt(0)
	v_mfma_f32_16x16x32_bf16 v[56:59], v[30:33], v[56:59], 0
	v_mfma_f32_16x16x32_bf16 v[48:51], v[40:43], v[48:51], v[56:59]
	s_nop 7
	v_cndmask_b32_e64 v35, v51, 0, s[40:41]
	v_cndmask_b32_e64 v141, v50, 0, s[62:63]
	v_cndmask_b32_e64 v170, v49, 0, s[72:73]
	v_cndmask_b32_e64 v171, v48, 0, s[2:3]
	v_mfma_f32_16x16x32_bf16 v[48:51], v[30:33], v[52:55], 0
	v_mfma_f32_16x16x32_bf16 v[56:59], v[40:43], v[64:67], v[48:51]
	v_mfma_f32_16x16x32_bf16 v[48:51], v[30:33], v[142:145], 0
	v_mfma_f32_16x16x32_bf16 v[30:33], v[30:33], v[158:161], 0
	v_mfma_f32_16x16x32_bf16 v[48:51], v[40:43], v[150:153], v[48:51]
	v_mfma_f32_16x16x32_bf16 v[40:43], v[40:43], v[166:169], v[30:33]
	v_mfma_f32_16x16x32_bf16 v[30:33], v[44:47], v[52:55], 0
	v_mfma_f32_16x16x32_bf16 v[30:33], v[60:63], v[64:67], v[30:33]
	v_cvt_pk_bf16_f32 v64, v26, v27
	v_cvt_pk_bf16_f32 v65, v28, v29
	v_cvt_pk_bf16_f32 v66, v36, v37
	v_cvt_pk_bf16_f32 v67, v38, v39
	s_nop 3
	v_cndmask_b32_e64 v172, v33, 0, s[40:41]
	v_cndmask_b32_e64 v173, v32, 0, s[62:63]
	v_cndmask_b32_e64 v174, v31, 0, s[72:73]
	v_cndmask_b32_e64 v175, v30, 0, s[2:3]
	v_mfma_f32_16x16x32_bf16 v[30:33], v[44:47], v[142:145], 0
	v_mfma_f32_16x16x32_bf16 v[68:71], v[60:63], v[150:153], v[30:33]
	v_mfma_f32_16x16x32_bf16 v[30:33], v[44:47], v[158:161], 0
	v_mfma_f32_16x16x32_bf16 v[52:55], v[60:63], v[166:169], v[30:33]
	v_cvt_pk_bf16_f32 v60, v18, v19
	v_cvt_pk_bf16_f32 v61, v20, v21
	v_cvt_pk_bf16_f32 v62, v22, v23
	v_mfma_f32_16x16x32_bf16 v[30:33], v[72:75], v[142:145], 0
	v_cvt_pk_bf16_f32 v63, v24, v25
	v_mfma_f32_16x16x32_bf16 v[30:33], v[146:149], v[150:153], v[30:33]
	s_nop 7
	v_cndmask_b32_e64 v150, v33, 0, s[40:41]
	v_cndmask_b32_e64 v151, v32, 0, s[62:63]
	v_cndmask_b32_e64 v152, v31, 0, s[72:73]
	v_cndmask_b32_e64 v153, v30, 0, s[2:3]
	v_mfma_f32_16x16x32_bf16 v[30:33], v[72:75], v[158:161], 0
	v_mfma_f32_16x16x32_bf16 v[44:47], v[146:149], v[166:169], v[30:33]
	v_mfma_f32_16x16x32_bf16 v[30:33], v[154:157], v[158:161], 0
	v_mfma_f32_16x16x32_bf16 v[30:33], v[162:165], v[166:169], v[30:33]
	s_nop 7
	v_cndmask_b32_e64 v157, v30, 0, s[2:3]
	v_add_u32_e32 v30, 0x6800, v106
	ds_read2_b64 v[142:145], v30 offset0:128 offset1:132
	ds_read2_b64 v[72:75], v30 offset0:136 offset1:140
	v_cndmask_b32_e64 v154, v33, 0, s[40:41]
	v_cndmask_b32_e64 v155, v32, 0, s[62:63]
	v_cvt_pk_bf16_f32 v32, v171, v170
	v_cvt_pk_bf16_f32 v33, v141, v35
	v_mov_b32_e32 v35, v34
	ds_read2_b64 v[146:149], v101 offset1:4
	v_cndmask_b32_e64 v156, v31, 0, s[72:73]
	s_waitcnt lgkmcnt(2)
	v_mfma_f32_16x16x32_bf16 v[30:33], v[142:145], v[32:35], 0
	s_waitcnt lgkmcnt(0)
	v_mfma_f32_16x16x32_bf16 v[30:33], v[60:63], v[146:149], v[30:33]
	ds_read2_b64 v[146:149], v101 offset0:8 offset1:12
	s_waitcnt lgkmcnt(0)
	v_mfma_f32_16x16x32_bf16 v[30:33], v[64:67], v[146:149], v[30:33]
	s_nop 7
	v_med3_f32 v30, v30, s75, v238
	v_med3_f32 v31, v31, s75, v238
	v_med3_f32 v32, v32, s75, v238
	v_med3_f32 v33, v33, s75, v238
	v_cvt_pk_fp8_f32 v247, v30, v31
	s_nop 1
	v_cvt_pk_fp8_f32 v247, v32, v33 op_sel:[0,0,1]
	s_nop 1
	global_store_dword v251, v247, s[94:95]
	v_cvt_pk_bf16_f32 v30, v56, v57
	v_cvt_pk_bf16_f32 v31, v58, v59
	v_cvt_pk_bf16_f32 v32, v175, v174
	v_cvt_pk_bf16_f32 v33, v173, v172
	ds_read2_b64 v[56:59], v102 offset1:4
	s_nop 0
	v_mfma_f32_16x16x32_bf16 v[30:33], v[142:145], v[30:33], 0
	s_waitcnt lgkmcnt(0)
	v_mfma_f32_16x16x32_bf16 v[30:33], v[60:63], v[56:59], v[30:33]
	ds_read2_b64 v[56:59], v102 offset0:8 offset1:12
	s_waitcnt lgkmcnt(0)
	v_mfma_f32_16x16x32_bf16 v[30:33], v[64:67], v[56:59], v[30:33]
	s_nop 7
	v_med3_f32 v30, v30, s75, v238
	v_med3_f32 v31, v31, s75, v238
	v_med3_f32 v32, v32, s75, v238
	v_med3_f32 v33, v33, s75, v238
	v_cvt_pk_fp8_f32 v248, v30, v31
	s_nop 1
	v_cvt_pk_fp8_f32 v248, v32, v33 op_sel:[0,0,1]
	s_nop 1
	global_store_dword v252, v248, s[94:95]
	v_cvt_pk_bf16_f32 v30, v48, v49
	v_cvt_pk_bf16_f32 v31, v50, v51
	v_cvt_pk_bf16_f32 v32, v68, v69
	v_cvt_pk_bf16_f32 v33, v70, v71
	s_nop 1
	v_mfma_f32_16x16x32_bf16 v[48:51], v[142:145], v[30:33], 0
	v_cvt_pk_bf16_f32 v32, v153, v152
	v_cvt_pk_bf16_f32 v33, v151, v150
	s_nop 1
	v_mfma_f32_16x16x32_bf16 v[30:33], v[72:75], v[32:35], v[48:51]
	v_add_u32_e32 v35, v95, v105
	s_nop 1
	ds_read2_b64 v[48:51], v103 offset1:4
	s_waitcnt lgkmcnt(0)
	v_mfma_f32_16x16x32_bf16 v[30:33], v[60:63], v[48:51], v[30:33]
	ds_read2_b64 v[48:51], v103 offset0:8 offset1:12
	s_waitcnt lgkmcnt(0)
	v_mfma_f32_16x16x32_bf16 v[30:33], v[64:67], v[48:51], v[30:33]
	s_nop 7
	v_med3_f32 v30, v30, s75, v238
	v_med3_f32 v31, v31, s75, v238
	v_med3_f32 v32, v32, s75, v238
	v_med3_f32 v33, v33, s75, v238
	v_cvt_pk_fp8_f32 v249, v30, v31
	s_nop 1
	v_cvt_pk_fp8_f32 v249, v32, v33 op_sel:[0,0,1]
	s_nop 1
	global_store_dword v253, v249, s[94:95]
	v_cvt_pk_bf16_f32 v30, v40, v41
	v_cvt_pk_bf16_f32 v31, v42, v43
	v_cvt_pk_bf16_f32 v32, v52, v53
	v_cvt_pk_bf16_f32 v33, v54, v55
	v_cvt_pk_bf16_f32 v40, v44, v45
	v_cvt_pk_bf16_f32 v41, v46, v47
	v_mfma_f32_16x16x32_bf16 v[30:33], v[142:145], v[30:33], 0
	v_cvt_pk_bf16_f32 v42, v157, v156
	v_cvt_pk_bf16_f32 v43, v155, v154
	v_add_u32_e32 v44, v95, v100
	s_nop 0
	v_mfma_f32_16x16x32_bf16 v[30:33], v[72:75], v[40:43], v[30:33]
	ds_read2_b64 v[40:43], v104 offset1:4
	s_waitcnt lgkmcnt(0)
	v_mfma_f32_16x16x32_bf16 v[30:33], v[60:63], v[40:43], v[30:33]
	ds_read2_b64 v[40:43], v104 offset0:8 offset1:12
	s_waitcnt lgkmcnt(0)
	v_mfma_f32_16x16x32_bf16 v[30:33], v[64:67], v[40:43], v[30:33]
	s_nop 7
	v_med3_f32 v30, v30, s75, v238
	v_med3_f32 v31, v31, s75, v238
	v_med3_f32 v32, v32, s75, v238
	v_med3_f32 v33, v33, s75, v238
	v_cvt_pk_fp8_f32 v250, v30, v31
	s_nop 1
	v_cvt_pk_fp8_f32 v250, v32, v33 op_sel:[0,0,1]
	s_nop 1
	global_store_dword v216, v250, s[94:95]
	ds_read_b128 v[30:33], v114 offset:48128
	ds_read_b128 v[40:43], v44 offset:18432
	s_waitcnt lgkmcnt(1)
	v_pk_mul_f32 v[18:19], v[18:19], v[30:31]
	v_pk_mul_f32 v[20:21], v[20:21], v[32:33]
	ds_read_b128 v[30:33], v114 offset:48192
	s_waitcnt lgkmcnt(0)
	v_pk_mul_f32 v[22:23], v[22:23], v[30:31]
	v_pk_mul_f32 v[24:25], v[24:25], v[32:33]
	ds_read_b128 v[30:33], v114 offset:48256
	s_waitcnt lgkmcnt(0)
	v_pk_mul_f32 v[26:27], v[26:27], v[30:31]
	v_pk_mul_f32 v[28:29], v[28:29], v[32:33]
	ds_read_b128 v[30:33], v114 offset:48320
	s_waitcnt lgkmcnt(0)
	v_pk_mul_f32 v[30:31], v[36:37], v[30:31]
	v_pk_mul_f32 v[32:33], v[38:39], v[32:33]
	ds_read_b128 v[36:39], v35 offset:27648
	s_waitcnt vmcnt(38)
	v_mov_b32_e32 v115, v178
	v_mov_b32_e32 v116, v179
	v_mov_b32_e32 v117, v180
	v_mov_b32_e32 v118, v181
	v_mov_b32_e32 v119, v182
	v_mov_b32_e32 v120, v183
	s_waitcnt lgkmcnt(0)
	v_mfma_f32_16x16x32_bf16 v[18:21], v[40:43], v[36:39], v[18:21]
	ds_read_b128 v[40:43], v44 offset:20736
	s_waitcnt vmcnt(32)
	v_mov_b32_e32 v121, v184
	v_mov_b32_e32 v122, v185
	v_mov_b32_e32 v123, v186
	v_mov_b32_e32 v124, v187
	v_mov_b32_e32 v125, v188
	v_mov_b32_e32 v128, v189
	s_waitcnt lgkmcnt(0)
	v_mfma_f32_16x16x32_bf16 v[22:25], v[40:43], v[36:39], v[22:25]
	ds_read_b128 v[40:43], v44 offset:23040
	s_waitcnt vmcnt(26)
	v_mov_b32_e32 v129, v190
	v_mov_b32_e32 v130, v192
	v_mov_b32_e32 v131, v194
	v_mov_b32_e32 v132, v196
	v_mov_b32_e32 v133, v200
	v_mov_b32_e32 v134, v201
	s_waitcnt lgkmcnt(0)
	v_mfma_f32_16x16x32_bf16 v[26:29], v[40:43], v[36:39], v[26:29]
	ds_read_b128 v[40:43], v44 offset:25344
	s_waitcnt vmcnt(20)
	v_mov_b32_e32 v135, v202
	v_mov_b32_e32 v136, v203
	v_mov_b32_e32 v137, v206
	v_mov_b32_e32 v138, v207
	v_mov_b32_e32 v139, v208
	v_mov_b32_e32 v140, v209
	s_waitcnt lgkmcnt(0)
	v_mfma_f32_16x16x32_bf16 v[30:33], v[40:43], v[36:39], v[30:33]
	ds_read_b128 v[36:39], v35 offset:27712
	ds_read_b128 v[40:43], v44 offset:18496
	s_waitcnt vmcnt(16)
	v_mov_b32_e32 v2, v220
	v_mov_b32_e32 v1, v219
	v_mov_b32_e32 v4, v222
	v_mov_b32_e32 v3, v221
	s_waitcnt lgkmcnt(0)
	v_mfma_f32_16x16x32_bf16 v[18:21], v[40:43], v[36:39], v[18:21]
	ds_read_b128 v[40:43], v44 offset:20800
	s_waitcnt vmcnt(12)
	v_mov_b32_e32 v6, v224
	v_mov_b32_e32 v5, v223
	v_mov_b32_e32 v8, v226
	v_mov_b32_e32 v7, v225
	s_waitcnt lgkmcnt(0)
	v_mfma_f32_16x16x32_bf16 v[22:25], v[40:43], v[36:39], v[22:25]
	ds_read_b128 v[40:43], v44 offset:23104
	s_waitcnt vmcnt(8)
	v_mov_b32_e32 v10, v228
	v_mov_b32_e32 v9, v227
	v_mov_b32_e32 v12, v230
	v_mov_b32_e32 v11, v229
	s_waitcnt lgkmcnt(0)
	v_mfma_f32_16x16x32_bf16 v[26:29], v[40:43], v[36:39], v[26:29]
	ds_read_b128 v[40:43], v44 offset:25408
	s_waitcnt vmcnt(4)
	v_mov_b32_e32 v14, v232
	v_mov_b32_e32 v13, v231
	v_mov_b32_e32 v16, v246
	v_mov_b32_e32 v15, v233
	s_waitcnt lgkmcnt(0)
	v_mfma_f32_16x16x32_bf16 v[36:39], v[40:43], v[36:39], v[30:33]
	s_nop 2
	s_branch .LBB0_468
